# C1 + grid barriers: each workgroup issues its acquire (buffer_inv sc1, this CU's L1) right after arriving instead of after the release is seen; no cached loads run on the CU in between, so the invalid
# baseline (speedup 1.0000x reference)
.LBB0_63:
	s_or_b64 exec, exec, s[10:11]
	v_cvt_f32_u32_e32 v5, v3
	s_waitcnt vmcnt(0)
	v_readfirstlane_b32 s3, v4
	v_sub_u32_e32 v4, 0, v3
	v_rcp_iflag_f32_e32 v5, v5
	v_add_u32_e32 v6, s3, v2
	v_mul_f32_e32 v5, 0x4f7ffffe, v5
	v_cvt_u32_f32_e32 v5, v5
	v_mul_lo_u32 v2, v4, v5
	v_mul_hi_u32 v2, v5, v2
	v_add_u32_e32 v2, v5, v2
	v_mul_hi_u32 v2, v6, v2
	v_mul_lo_u32 v4, v2, v3
	v_sub_u32_e32 v4, v6, v4
	v_add_u32_e32 v5, 1, v2
	v_cmp_ge_u32_e32 vcc, v4, v3
	s_nop 1
	v_cndmask_b32_e32 v2, v2, v5, vcc
	v_sub_u32_e32 v5, v4, v3
	v_cndmask_b32_e32 v4, v4, v5, vcc
	v_add_u32_e32 v5, 1, v2
	v_cmp_ge_u32_e32 vcc, v4, v3
	v_add_u32_e32 v4, 1, v6
	s_nop 0
	v_cndmask_b32_e32 v2, v2, v5, vcc
	v_mul_lo_u32 v5, v3, v2
	v_add_u32_e32 v3, v5, v3
	v_cmp_ne_u32_e32 vcc, v4, v3
	s_and_saveexec_b64 s[8:9], vcc
	s_xor_b64 s[8:9], exec, s[8:9]
	s_cbranch_execz .LBB0_77
	s_waitcnt lgkmcnt(0)
	buffer_inv sc1
	v_mov_b32_e32 v1, 0x2000
	global_load_dword v1, v1, s[6:7] offset:1024 sc1
	s_add_u32 s14, s6, 0x2400
	s_addc_u32 s15, s7, 0
	s_waitcnt vmcnt(0)
	v_cmp_eq_u32_e32 vcc, v1, v2
	s_and_saveexec_b64 s[10:11], vcc
	s_cbranch_execz .LBB0_76
	s_add_u32 s12, s26, 0x4200
	s_addc_u32 s13, s27, 0
	s_mov_b32 s3, 1
	s_mov_b64 s[16:17], 0
	v_mov_b32_e32 v1, 0
	s_branch .LBB0_67

.LBB0_76:
	s_or_b64 exec, exec, s[10:11]
	s_waitcnt vmcnt(0)
	s_waitcnt vmcnt(0)
.LBB0_77:
	s_andn2_saveexec_b64 s[8:9], s[8:9]
	s_cbranch_execz .LBB0_97
	s_mov_b64 s[8:9], exec
	buffer_wbl2 sc1
	s_waitcnt lgkmcnt(0)
	s_waitcnt vmcnt(0)
	buffer_inv sc1
	v_mbcnt_lo_u32_b32 v2, s8, 0
	v_mbcnt_hi_u32_b32 v2, s9, v2
	v_cmp_eq_u32_e32 vcc, 0, v2
	s_and_saveexec_b64 s[10:11], vcc
	s_cbranch_execz .LBB0_80
	s_bcnt1_i32_b64 s3, s[8:9]
	v_mov_b32_e32 v3, 0x7000
	v_mov_b32_e32 v4, s3
	global_atomic_add v3, v3, v4, s[26:27] offset:1024 sc0

.LBB0_94:
	s_or_b64 exec, exec, s[8:9]
	s_mov_b64 s[8:9], exec
	v_mbcnt_lo_u32_b32 v1, s8, 0
	v_mbcnt_hi_u32_b32 v1, s9, v1
	v_cmp_eq_u32_e32 vcc, 0, v1
	s_waitcnt vmcnt(0)
	s_and_saveexec_b64 s[10:11], vcc
	s_cbranch_execz .LBB0_96
	s_bcnt1_i32_b64 s3, s[8:9]
	v_mov_b32_e32 v1, 0x2000
	v_mov_b32_e32 v2, s3
	global_atomic_add v1, v2, s[6:7] offset:1024

.LBB0_158:
	s_or_b64 exec, exec, s[12:13]
	v_cvt_f32_u32_e32 v5, v3
	s_waitcnt vmcnt(0)
	v_readfirstlane_b32 s3, v4
	v_sub_u32_e32 v4, 0, v3
	v_rcp_iflag_f32_e32 v5, v5
	v_add_u32_e32 v6, s3, v2
	v_mul_f32_e32 v5, 0x4f7ffffe, v5
	v_cvt_u32_f32_e32 v5, v5
	v_mul_lo_u32 v2, v4, v5
	v_mul_hi_u32 v2, v5, v2
	v_add_u32_e32 v2, v5, v2
	v_mul_hi_u32 v2, v6, v2
	v_mul_lo_u32 v4, v2, v3
	v_sub_u32_e32 v4, v6, v4
	v_add_u32_e32 v5, 1, v2
	v_cmp_ge_u32_e32 vcc, v4, v3
	s_nop 1
	v_cndmask_b32_e32 v2, v2, v5, vcc
	v_sub_u32_e32 v5, v4, v3
	v_cndmask_b32_e32 v4, v4, v5, vcc
	v_add_u32_e32 v5, 1, v2
	v_cmp_ge_u32_e32 vcc, v4, v3
	v_add_u32_e32 v4, 1, v6
	s_nop 0
	v_cndmask_b32_e32 v2, v2, v5, vcc
	v_mul_lo_u32 v5, v3, v2
	v_add_u32_e32 v3, v5, v3
	v_cmp_ne_u32_e32 vcc, v4, v3
	s_and_saveexec_b64 s[10:11], vcc
	s_xor_b64 s[10:11], exec, s[10:11]
	s_cbranch_execz .LBB0_172
	s_waitcnt lgkmcnt(0)
	buffer_inv sc1
	v_mov_b32_e32 v1, 0x2000
	global_load_dword v1, v1, s[8:9] offset:1024 sc1
	s_add_u32 s16, s8, 0x2400
	s_addc_u32 s17, s9, 0
	s_waitcnt vmcnt(0)
	v_cmp_eq_u32_e32 vcc, v1, v2
	s_and_saveexec_b64 s[12:13], vcc
	s_cbranch_execz .LBB0_171
	s_add_u32 s14, s26, 0x4200
	s_addc_u32 s15, s27, 0
	s_mov_b32 s3, 1
	s_mov_b64 s[18:19], 0
	v_mov_b32_e32 v1, 0
	s_branch .LBB0_162

.LBB0_171:
	s_or_b64 exec, exec, s[12:13]
	s_waitcnt vmcnt(0)
	s_waitcnt vmcnt(0)
.LBB0_172:
	s_andn2_saveexec_b64 s[10:11], s[10:11]
	s_cbranch_execz .LBB0_192
	s_mov_b64 s[10:11], exec
	buffer_wbl2 sc1
	s_waitcnt lgkmcnt(0)
	s_waitcnt vmcnt(0)
	buffer_inv sc1
	v_mbcnt_lo_u32_b32 v2, s10, 0
	v_mbcnt_hi_u32_b32 v2, s11, v2
	v_cmp_eq_u32_e32 vcc, 0, v2
	s_and_saveexec_b64 s[12:13], vcc
	s_cbranch_execz .LBB0_175
	s_bcnt1_i32_b64 s3, s[10:11]
	v_mov_b32_e32 v3, 0x7000
	v_mov_b32_e32 v4, s3
	global_atomic_add v3, v3, v4, s[26:27] offset:1024 sc0

.LBB0_189:
	s_or_b64 exec, exec, s[10:11]
	s_mov_b64 s[10:11], exec
	v_mbcnt_lo_u32_b32 v1, s10, 0
	v_mbcnt_hi_u32_b32 v1, s11, v1
	v_cmp_eq_u32_e32 vcc, 0, v1
	s_waitcnt vmcnt(0)
	s_and_saveexec_b64 s[12:13], vcc
	s_cbranch_execz .LBB0_191
	s_bcnt1_i32_b64 s3, s[10:11]
	v_mov_b32_e32 v1, 0x2000
	v_mov_b32_e32 v2, s3
	global_atomic_add v1, v2, s[8:9] offset:1024

.LBB0_612:
	s_or_b64 exec, exec, s[10:11]
	v_cvt_f32_u32_e32 v5, v3
	s_waitcnt vmcnt(0)
	v_readfirstlane_b32 s2, v4
	v_sub_u32_e32 v4, 0, v3
	v_rcp_iflag_f32_e32 v5, v5
	v_add_u32_e32 v6, s2, v2
	v_mul_f32_e32 v5, 0x4f7ffffe, v5
	v_cvt_u32_f32_e32 v5, v5
	v_mul_lo_u32 v2, v4, v5
	v_mul_hi_u32 v2, v5, v2
	v_add_u32_e32 v2, v5, v2
	v_mul_hi_u32 v2, v6, v2
	v_mul_lo_u32 v4, v2, v3
	v_sub_u32_e32 v4, v6, v4
	v_add_u32_e32 v5, 1, v2
	v_cmp_ge_u32_e32 vcc, v4, v3
	s_nop 1
	v_cndmask_b32_e32 v2, v2, v5, vcc
	v_sub_u32_e32 v5, v4, v3
	v_cndmask_b32_e32 v4, v4, v5, vcc
	v_add_u32_e32 v5, 1, v2
	v_cmp_ge_u32_e32 vcc, v4, v3
	v_add_u32_e32 v4, 1, v6
	s_nop 0
	v_cndmask_b32_e32 v2, v2, v5, vcc
	v_mul_lo_u32 v5, v3, v2
	v_add_u32_e32 v3, v5, v3
	v_cmp_ne_u32_e32 vcc, v4, v3
	s_and_saveexec_b64 s[8:9], vcc
	s_xor_b64 s[8:9], exec, s[8:9]
	s_cbranch_execz .LBB0_626
	s_waitcnt lgkmcnt(0)
	buffer_inv sc1
	v_mov_b32_e32 v1, 0x2000
	global_load_dword v1, v1, s[6:7] offset:1024 sc1
	s_add_u32 s18, s6, 0x2400
	s_addc_u32 s19, s7, 0
	s_waitcnt vmcnt(0)
	v_cmp_eq_u32_e32 vcc, v1, v2
	s_and_saveexec_b64 s[10:11], vcc
	s_cbranch_execz .LBB0_625
	s_add_u32 s12, s26, 0x4200
	s_addc_u32 s13, s27, 0
	s_mov_b32 s20, 1
	s_mov_b64 s[30:31], 0
	v_mov_b32_e32 v1, 0
	s_branch .LBB0_616

.LBB0_626:
	s_andn2_saveexec_b64 s[8:9], s[8:9]
	s_cbranch_execz .LBB0_646
	s_mov_b64 s[8:9], exec
	buffer_wbl2 sc1
	s_waitcnt lgkmcnt(0)
	s_waitcnt vmcnt(0)
	buffer_inv sc1
	v_mbcnt_lo_u32_b32 v2, s8, 0
	v_mbcnt_hi_u32_b32 v2, s9, v2
	v_cmp_eq_u32_e32 vcc, 0, v2
	s_and_saveexec_b64 s[10:11], vcc
	s_cbranch_execz .LBB0_629
	s_bcnt1_i32_b64 s2, s[8:9]
	v_mov_b32_e32 v3, 0x7000
	v_mov_b32_e32 v4, s2
	global_atomic_add v3, v3, v4, s[26:27] offset:1024 sc0

.LBB0_643:
	s_or_b64 exec, exec, s[8:9]
	s_mov_b64 s[8:9], exec
	v_mbcnt_lo_u32_b32 v1, s8, 0
	v_mbcnt_hi_u32_b32 v1, s9, v1
	v_cmp_eq_u32_e32 vcc, 0, v1
	s_waitcnt vmcnt(0)
	s_and_saveexec_b64 s[10:11], vcc
	s_cbranch_execz .LBB0_645
	s_bcnt1_i32_b64 s2, s[8:9]
	v_mov_b32_e32 v1, 0x2000
	v_mov_b32_e32 v2, s2
	global_atomic_add v1, v2, s[6:7] offset:1024

.LBB0_826:
	s_or_b64 exec, exec, s[10:11]
	v_cvt_f32_u32_e32 v5, v3
	s_waitcnt vmcnt(0)
	v_readfirstlane_b32 s2, v4
	v_sub_u32_e32 v4, 0, v3
	v_rcp_iflag_f32_e32 v5, v5
	v_add_u32_e32 v6, s2, v2
	v_mul_f32_e32 v5, 0x4f7ffffe, v5
	v_cvt_u32_f32_e32 v5, v5
	v_mul_lo_u32 v2, v4, v5
	v_mul_hi_u32 v2, v5, v2
	v_add_u32_e32 v2, v5, v2
	v_mul_hi_u32 v2, v6, v2
	v_mul_lo_u32 v4, v2, v3
	v_sub_u32_e32 v4, v6, v4
	v_add_u32_e32 v5, 1, v2
	v_cmp_ge_u32_e32 vcc, v4, v3
	s_nop 1
	v_cndmask_b32_e32 v2, v2, v5, vcc
	v_sub_u32_e32 v5, v4, v3
	v_cndmask_b32_e32 v4, v4, v5, vcc
	v_add_u32_e32 v5, 1, v2
	v_cmp_ge_u32_e32 vcc, v4, v3
	v_add_u32_e32 v4, 1, v6
	s_nop 0
	v_cndmask_b32_e32 v2, v2, v5, vcc
	v_mul_lo_u32 v5, v3, v2
	v_add_u32_e32 v3, v5, v3
	v_cmp_ne_u32_e32 vcc, v4, v3
	s_and_saveexec_b64 s[8:9], vcc
	s_xor_b64 s[8:9], exec, s[8:9]
	s_cbranch_execz .LBB0_840
	s_waitcnt lgkmcnt(0)
	buffer_inv sc1
	v_mov_b32_e32 v1, 0x2000
	global_load_dword v1, v1, s[6:7] offset:1024 sc1
	s_add_u32 s18, s6, 0x2400
	s_addc_u32 s19, s7, 0
	s_waitcnt vmcnt(0)
	v_cmp_eq_u32_e32 vcc, v1, v2
	s_and_saveexec_b64 s[10:11], vcc
	s_cbranch_execz .LBB0_839
	s_add_u32 s12, s26, 0x4200
	s_addc_u32 s13, s27, 0
	s_mov_b32 s3, 1
	s_mov_b64 s[20:21], 0
	v_mov_b32_e32 v1, 0
	s_branch .LBB0_830

.LBB0_1005:
	s_or_b64 exec, exec, s[10:11]
	v_cvt_f32_u32_e32 v5, v3
	s_waitcnt vmcnt(0)
	v_readfirstlane_b32 s2, v4
	v_sub_u32_e32 v4, 0, v3
	v_rcp_iflag_f32_e32 v5, v5
	v_add_u32_e32 v6, s2, v2
	v_mul_f32_e32 v5, 0x4f7ffffe, v5
	v_cvt_u32_f32_e32 v5, v5
	v_mul_lo_u32 v2, v4, v5
	v_mul_hi_u32 v2, v5, v2
	v_add_u32_e32 v2, v5, v2
	v_mul_hi_u32 v2, v6, v2
	v_mul_lo_u32 v4, v2, v3
	v_sub_u32_e32 v4, v6, v4
	v_add_u32_e32 v5, 1, v2
	v_cmp_ge_u32_e32 vcc, v4, v3
	s_nop 1
	v_cndmask_b32_e32 v2, v2, v5, vcc
	v_sub_u32_e32 v5, v4, v3
	v_cndmask_b32_e32 v4, v4, v5, vcc
	v_add_u32_e32 v5, 1, v2
	v_cmp_ge_u32_e32 vcc, v4, v3
	v_add_u32_e32 v4, 1, v6
	s_nop 0
	v_cndmask_b32_e32 v2, v2, v5, vcc
	v_mul_lo_u32 v5, v3, v2
	v_add_u32_e32 v3, v5, v3
	v_cmp_ne_u32_e32 vcc, v4, v3
	s_and_saveexec_b64 s[8:9], vcc
	s_xor_b64 s[8:9], exec, s[8:9]
	s_cbranch_execz .LBB0_1019
	s_waitcnt lgkmcnt(0)
	buffer_inv sc1
	v_mov_b32_e32 v1, 0x2000
	global_load_dword v1, v1, s[6:7] offset:1024 sc1
	s_add_u32 s16, s6, 0x2400
	s_addc_u32 s17, s7, 0
	s_waitcnt vmcnt(0)
	v_cmp_eq_u32_e32 vcc, v1, v2
	s_and_saveexec_b64 s[10:11], vcc
	s_cbranch_execz .LBB0_1018
	s_add_u32 s12, s26, 0x4200
	s_addc_u32 s13, s27, 0
	s_mov_b32 s3, 1
	s_mov_b64 s[18:19], 0
	v_mov_b32_e32 v1, 0
	s_branch .LBB0_1009

.LBB0_1067:
	s_or_b64 exec, exec, s[10:11]
	v_cvt_f32_u32_e32 v5, v3
	s_waitcnt vmcnt(0)
	v_readfirstlane_b32 s2, v4
	v_sub_u32_e32 v4, 0, v3
	v_rcp_iflag_f32_e32 v5, v5
	v_add_u32_e32 v6, s2, v2
	v_mul_f32_e32 v5, 0x4f7ffffe, v5
	v_cvt_u32_f32_e32 v5, v5
	v_mul_lo_u32 v2, v4, v5
	v_mul_hi_u32 v2, v5, v2
	v_add_u32_e32 v2, v5, v2
	v_mul_hi_u32 v2, v6, v2
	v_mul_lo_u32 v4, v2, v3
	v_sub_u32_e32 v4, v6, v4
	v_add_u32_e32 v5, 1, v2
	v_cmp_ge_u32_e32 vcc, v4, v3
	s_nop 1
	v_cndmask_b32_e32 v2, v2, v5, vcc
	v_sub_u32_e32 v5, v4, v3
	v_cndmask_b32_e32 v4, v4, v5, vcc
	v_add_u32_e32 v5, 1, v2
	v_cmp_ge_u32_e32 vcc, v4, v3
	v_add_u32_e32 v4, 1, v6
	s_nop 0
	v_cndmask_b32_e32 v2, v2, v5, vcc
	v_mul_lo_u32 v5, v3, v2
	v_add_u32_e32 v3, v5, v3
	v_cmp_ne_u32_e32 vcc, v4, v3
	s_and_saveexec_b64 s[8:9], vcc
	s_xor_b64 s[8:9], exec, s[8:9]
	s_cbranch_execz .LBB0_1081
	s_waitcnt lgkmcnt(0)
	buffer_inv sc1
	v_mov_b32_e32 v1, 0x2000
	global_load_dword v1, v1, s[6:7] offset:1024 sc1
	s_add_u32 s14, s6, 0x2400
	s_addc_u32 s15, s7, 0
	s_waitcnt vmcnt(0)
	v_cmp_eq_u32_e32 vcc, v1, v2
	s_and_saveexec_b64 s[10:11], vcc
	s_cbranch_execz .LBB0_1080
	s_add_u32 s12, s26, 0x4200
	s_addc_u32 s13, s27, 0
	s_mov_b32 s3, 1
	s_mov_b64 s[16:17], 0
	v_mov_b32_e32 v1, 0
	s_branch .LBB0_1071

.LBB0_1164:
	s_or_b64 exec, exec, s[10:11]
	v_cvt_f32_u32_e32 v5, v3
	s_waitcnt vmcnt(0)
	v_readfirstlane_b32 s2, v4
	v_sub_u32_e32 v4, 0, v3
	v_rcp_iflag_f32_e32 v5, v5
	v_add_u32_e32 v6, s2, v2
	v_mul_f32_e32 v5, 0x4f7ffffe, v5
	v_cvt_u32_f32_e32 v5, v5
	v_mul_lo_u32 v2, v4, v5
	v_mul_hi_u32 v2, v5, v2
	v_add_u32_e32 v2, v5, v2
	v_mul_hi_u32 v2, v6, v2
	v_mul_lo_u32 v4, v2, v3
	v_sub_u32_e32 v4, v6, v4
	v_add_u32_e32 v5, 1, v2
	v_cmp_ge_u32_e32 vcc, v4, v3
	s_nop 1
	v_cndmask_b32_e32 v2, v2, v5, vcc
	v_sub_u32_e32 v5, v4, v3
	v_cndmask_b32_e32 v4, v4, v5, vcc
	v_add_u32_e32 v5, 1, v2
	v_cmp_ge_u32_e32 vcc, v4, v3
	v_add_u32_e32 v4, 1, v6
	s_nop 0
	v_cndmask_b32_e32 v2, v2, v5, vcc
	v_mul_lo_u32 v5, v3, v2
	v_add_u32_e32 v3, v5, v3
	v_cmp_ne_u32_e32 vcc, v4, v3
	s_and_saveexec_b64 s[8:9], vcc
	s_xor_b64 s[8:9], exec, s[8:9]
	s_cbranch_execz .LBB0_1178
	s_waitcnt lgkmcnt(0)
	buffer_inv sc1
	v_mov_b32_e32 v1, 0x2000
	global_load_dword v1, v1, s[4:5] offset:1024 sc1
	s_add_u32 s16, s4, 0x2400
	s_addc_u32 s17, s5, 0
	s_waitcnt vmcnt(0)
	v_cmp_eq_u32_e32 vcc, v1, v2
	s_and_saveexec_b64 s[10:11], vcc
	s_cbranch_execz .LBB0_1177
	s_add_u32 s14, s26, 0x4200
	s_addc_u32 s15, s27, 0
	s_mov_b32 s3, 1
	s_mov_b64 s[18:19], 0
	v_mov_b32_e32 v1, 0
	s_branch .LBB0_1168

.LBB0_1195:
	s_or_b64 exec, exec, s[8:9]
	s_mov_b64 s[8:9], exec
	v_mbcnt_lo_u32_b32 v1, s8, 0
	v_mbcnt_hi_u32_b32 v1, s9, v1
	v_cmp_eq_u32_e32 vcc, 0, v1
	s_waitcnt vmcnt(0)
	s_and_saveexec_b64 s[10:11], vcc
	s_cbranch_execz .LBB0_1197
	s_bcnt1_i32_b64 s2, s[8:9]
	v_mov_b32_e32 v1, 0x2000
	v_mov_b32_e32 v2, s2
	global_atomic_add v1, v2, s[4:5] offset:1024

.LBB0_1263:
	s_or_b64 exec, exec, s[12:13]
	v_cvt_f32_u32_e32 v5, v3
	s_waitcnt vmcnt(0)
	v_readfirstlane_b32 s2, v4
	v_sub_u32_e32 v4, 0, v3
	v_rcp_iflag_f32_e32 v5, v5
	v_add_u32_e32 v6, s2, v2
	v_mul_f32_e32 v5, 0x4f7ffffe, v5
	v_cvt_u32_f32_e32 v5, v5
	v_mul_lo_u32 v2, v4, v5
	v_mul_hi_u32 v2, v5, v2
	v_add_u32_e32 v2, v5, v2
	v_mul_hi_u32 v2, v6, v2
	v_mul_lo_u32 v4, v2, v3
	v_sub_u32_e32 v4, v6, v4
	v_add_u32_e32 v5, 1, v2
	v_cmp_ge_u32_e32 vcc, v4, v3
	s_nop 1
	v_cndmask_b32_e32 v2, v2, v5, vcc
	v_sub_u32_e32 v5, v4, v3
	v_cndmask_b32_e32 v4, v4, v5, vcc
	v_add_u32_e32 v5, 1, v2
	v_cmp_ge_u32_e32 vcc, v4, v3
	v_add_u32_e32 v4, 1, v6
	s_nop 0
	v_cndmask_b32_e32 v2, v2, v5, vcc
	v_mul_lo_u32 v5, v3, v2
	v_add_u32_e32 v3, v5, v3
	v_cmp_ne_u32_e32 vcc, v4, v3
	s_and_saveexec_b64 s[10:11], vcc
	s_xor_b64 s[10:11], exec, s[10:11]
	s_cbranch_execz .LBB0_1277
	s_waitcnt lgkmcnt(0)
	buffer_inv sc1
	v_mov_b32_e32 v1, 0x2000
	global_load_dword v1, v1, s[8:9] offset:1024 sc1
	s_add_u32 s16, s8, 0x2400
	s_addc_u32 s17, s9, 0
	s_waitcnt vmcnt(0)
	v_cmp_eq_u32_e32 vcc, v1, v2
	s_and_saveexec_b64 s[12:13], vcc
	s_cbranch_execz .LBB0_1276
	s_add_u32 s14, s26, 0x4200
	s_addc_u32 s15, s27, 0
	s_mov_b32 s3, 1
	s_mov_b64 s[18:19], 0
	v_mov_b32_e32 v1, 0
	s_branch .LBB0_1267

.LBB0_1277:
	s_andn2_saveexec_b64 s[10:11], s[10:11]
	s_cbranch_execz .LBB0_1297
	s_mov_b64 s[10:11], exec
	buffer_wbl2 sc1
	s_waitcnt lgkmcnt(0)
	s_waitcnt vmcnt(0)
	buffer_inv sc1
	v_mbcnt_lo_u32_b32 v2, s10, 0
	v_mbcnt_hi_u32_b32 v2, s11, v2
	v_cmp_eq_u32_e32 vcc, 0, v2
	s_and_saveexec_b64 s[12:13], vcc
	s_cbranch_execz .LBB0_1280
	s_bcnt1_i32_b64 s2, s[10:11]
	v_mov_b32_e32 v3, 0x7000
	v_mov_b32_e32 v4, s2
	global_atomic_add v3, v3, v4, s[26:27] offset:1024 sc0

.LBB0_1294:
	s_or_b64 exec, exec, s[10:11]
	s_mov_b64 s[10:11], exec
	v_mbcnt_lo_u32_b32 v1, s10, 0
	v_mbcnt_hi_u32_b32 v1, s11, v1
	v_cmp_eq_u32_e32 vcc, 0, v1
	s_waitcnt vmcnt(0)
	s_and_saveexec_b64 s[12:13], vcc
	s_cbranch_execz .LBB0_1296
	s_bcnt1_i32_b64 s2, s[10:11]
	v_mov_b32_e32 v1, 0x2000
	v_mov_b32_e32 v2, s2
	global_atomic_add v1, v2, s[8:9] offset:1024

.LBB0_1432:
	s_or_b64 exec, exec, s[30:31]
	v_cvt_f32_u32_e32 v5, v3
	s_waitcnt vmcnt(0)
	v_readfirstlane_b32 s2, v4
	v_sub_u32_e32 v4, 0, v3
	v_rcp_iflag_f32_e32 v5, v5
	v_add_u32_e32 v6, s2, v2
	v_mul_f32_e32 v5, 0x4f7ffffe, v5
	v_cvt_u32_f32_e32 v5, v5
	v_mul_lo_u32 v2, v4, v5
	v_mul_hi_u32 v2, v5, v2
	v_add_u32_e32 v2, v5, v2
	v_mul_hi_u32 v2, v6, v2
	v_mul_lo_u32 v4, v2, v3
	v_sub_u32_e32 v4, v6, v4
	v_add_u32_e32 v5, 1, v2
	v_cmp_ge_u32_e32 vcc, v4, v3
	s_nop 1
	v_cndmask_b32_e32 v2, v2, v5, vcc
	v_sub_u32_e32 v5, v4, v3
	v_cndmask_b32_e32 v4, v4, v5, vcc
	v_add_u32_e32 v5, 1, v2
	v_cmp_ge_u32_e32 vcc, v4, v3
	v_add_u32_e32 v4, 1, v6
	s_nop 0
	v_cndmask_b32_e32 v2, v2, v5, vcc
	v_mul_lo_u32 v5, v3, v2
	v_add_u32_e32 v3, v5, v3
	v_cmp_ne_u32_e32 vcc, v4, v3
	s_and_saveexec_b64 s[18:19], vcc
	s_xor_b64 s[18:19], exec, s[18:19]
	s_cbranch_execz .LBB0_1446
	s_waitcnt lgkmcnt(0)
	buffer_inv sc1
	v_mov_b32_e32 v1, 0x2000
	global_load_dword v1, v1, s[10:11] offset:1024 sc1
	s_add_u32 s36, s10, 0x2400
	s_addc_u32 s37, s11, 0
	s_waitcnt vmcnt(0)
	v_cmp_eq_u32_e32 vcc, v1, v2
	s_and_saveexec_b64 s[30:31], vcc
	s_cbranch_execz .LBB0_1445
	s_add_u32 s34, s26, 0x4200
	s_addc_u32 s35, s27, 0
	s_mov_b32 s3, 1
	s_mov_b64 s[54:55], 0
	v_mov_b32_e32 v1, 0
	s_branch .LBB0_1436

.LBB0_1445:
	s_or_b64 exec, exec, s[30:31]
	s_waitcnt vmcnt(0)
	s_waitcnt vmcnt(0)
.LBB0_1446:
	s_andn2_saveexec_b64 s[18:19], s[18:19]
	s_cbranch_execz .LBB0_1466
	s_mov_b64 s[18:19], exec
	buffer_wbl2 sc1
	s_waitcnt lgkmcnt(0)
	s_waitcnt vmcnt(0)
	buffer_inv sc1
	v_mbcnt_lo_u32_b32 v2, s18, 0
	v_mbcnt_hi_u32_b32 v2, s19, v2
	v_cmp_eq_u32_e32 vcc, 0, v2
	s_and_saveexec_b64 s[30:31], vcc
	s_cbranch_execz .LBB0_1449
	s_bcnt1_i32_b64 s2, s[18:19]
	v_mov_b32_e32 v3, 0x7000
	v_mov_b32_e32 v4, s2
	global_atomic_add v3, v3, v4, s[26:27] offset:1024 sc0

.LBB0_1463:
	s_or_b64 exec, exec, s[18:19]
	s_mov_b64 s[18:19], exec
	v_mbcnt_lo_u32_b32 v1, s18, 0
	v_mbcnt_hi_u32_b32 v1, s19, v1
	v_cmp_eq_u32_e32 vcc, 0, v1
	s_waitcnt vmcnt(0)
	s_and_saveexec_b64 s[30:31], vcc
	s_cbranch_execz .LBB0_1465
	s_bcnt1_i32_b64 s2, s[18:19]
	v_mov_b32_e32 v1, 0x2000
	v_mov_b32_e32 v2, s2
	global_atomic_add v1, v2, s[10:11] offset:1024

.LBB0_1682:
	s_or_b64 exec, exec, s[8:9]
	v_cvt_f32_u32_e32 v4, v2
	s_waitcnt vmcnt(0)
	v_readfirstlane_b32 s6, v3
	v_sub_u32_e32 v3, 0, v2
	v_rcp_iflag_f32_e32 v4, v4
	v_add_u32_e32 v5, s6, v1
	v_mul_f32_e32 v4, 0x4f7ffffe, v4
	v_cvt_u32_f32_e32 v4, v4
	v_mul_lo_u32 v1, v3, v4
	v_mul_hi_u32 v1, v4, v1
	v_add_u32_e32 v1, v4, v1
	v_mul_hi_u32 v1, v5, v1
	v_mul_lo_u32 v3, v1, v2
	v_sub_u32_e32 v3, v5, v3
	v_add_u32_e32 v4, 1, v1
	v_cmp_ge_u32_e32 vcc, v3, v2
	s_nop 1
	v_cndmask_b32_e32 v1, v1, v4, vcc
	v_sub_u32_e32 v4, v3, v2
	v_cndmask_b32_e32 v3, v3, v4, vcc
	v_add_u32_e32 v4, 1, v1
	v_cmp_ge_u32_e32 vcc, v3, v2
	v_add_u32_e32 v3, 1, v5
	s_nop 0
	v_cndmask_b32_e32 v1, v1, v4, vcc
	v_mul_lo_u32 v4, v2, v1
	v_add_u32_e32 v2, v4, v2
	v_cmp_ne_u32_e32 vcc, v3, v2
	s_and_saveexec_b64 s[6:7], vcc
	s_xor_b64 s[6:7], exec, s[6:7]
	s_cbranch_execz .LBB0_1696
	s_waitcnt lgkmcnt(0)
	buffer_inv sc1
	v_mov_b32_e32 v0, 0x2000
	global_load_dword v0, v0, s[4:5] offset:1024 sc1
	s_add_u32 s12, s4, 0x2400
	s_addc_u32 s13, s5, 0
	s_waitcnt vmcnt(0)
	v_cmp_eq_u32_e32 vcc, v0, v1
	s_and_saveexec_b64 s[8:9], vcc
	s_cbranch_execz .LBB0_1695
	s_add_u32 s10, s26, 0x4200
	s_addc_u32 s11, s27, 0
	s_mov_b32 s22, 1
	s_mov_b64 s[14:15], 0
	v_mov_b32_e32 v0, 0
	s_branch .LBB0_1686

.LBB0_1695:
	s_or_b64 exec, exec, s[8:9]
	s_waitcnt vmcnt(0)
	s_waitcnt vmcnt(0)
.LBB0_1696:
	s_andn2_saveexec_b64 s[6:7], s[6:7]
	s_cbranch_execz .LBB0_1716
	s_mov_b64 s[6:7], exec
	buffer_wbl2 sc1
	s_waitcnt lgkmcnt(0)
	s_waitcnt vmcnt(0)
	buffer_inv sc1
	v_mbcnt_lo_u32_b32 v1, s6, 0
	v_mbcnt_hi_u32_b32 v1, s7, v1
	v_cmp_eq_u32_e32 vcc, 0, v1
	s_and_saveexec_b64 s[8:9], vcc
	s_cbranch_execz .LBB0_1699
	s_bcnt1_i32_b64 s6, s[6:7]
	v_mov_b32_e32 v2, 0x7000
	v_mov_b32_e32 v3, s6
	global_atomic_add v2, v2, v3, s[26:27] offset:1024 sc0

.LBB0_1713:
	s_or_b64 exec, exec, s[6:7]
	s_mov_b64 s[6:7], exec
	v_mbcnt_lo_u32_b32 v0, s6, 0
	v_mbcnt_hi_u32_b32 v0, s7, v0
	v_cmp_eq_u32_e32 vcc, 0, v0
	s_waitcnt vmcnt(0)
	s_and_saveexec_b64 s[8:9], vcc
	s_cbranch_execz .LBB0_1715
	s_bcnt1_i32_b64 s6, s[6:7]
	v_mov_b32_e32 v0, 0x2000
	v_mov_b32_e32 v1, s6
	global_atomic_add v0, v1, s[4:5] offset:1024
